# speedup vs baseline: 1.0059x; 1.0059x over previous
.Lmk_start:
	s_mov_b32 s28, s8
	s_mov_b64 s[30:31], s[4:5]
	s_mov_b64 s[32:33], s[6:7]
	s_mov_b64 s[6:7], s[2:3]
	s_mov_b64 s[34:35], s[2:3]
	s_mov_b32 s2, s28
	s_and_b32 s3, s2, 7
	s_lshr_b32 s4, s2, 3
	s_and_b32 s5, s4, 3
	s_lshl_b32 s3, s3, 2
	s_or_b32 s8, s3, s5
	s_lshr_b32 s9, s4, 2
	v_lshrrev_b32_e32 v127, 6, v0
	v_and_b32_e32 v124, 63, v0
	v_lshlrev_b32_e32 v124, 4, v124
	v_add_u32_e32 v125, 0xf000, v124
	v_readfirstlane_b32 s12, v127
	v_mov_b32_e32 v120, 0
	v_mov_b32_e32 v121, 0
	v_mov_b32_e32 v122, 0
	v_mov_b32_e32 v123, 0
	s_lshl_b32 s13, s12, 10
	s_lshl_b32 s14, s9, 3
	s_add_u32 s14, s14, s12
	s_mul_i32 s15, s14, 0x1800
	s_mul_i32 s16, s8, 0x12000
	s_add_u32 s16, s16, 0xc0000
	s_add_u32 s16, s16, s13
	s_add_u32 s20, s13, 0x2000
	s_add_u32 s10, s6, s16
	s_addc_u32 s11, s7, 0
	s_add_u32 s18, s6, s15
	s_addc_u32 s19, s7, 0
	s_add_u32 s22, s18, 0xc00
	s_addc_u32 s23, s19, 0
	s_cmp_lt_u32 s12, 4
	s_cbranch_scc0 .Lmk_vb
	s_mov_b32 m0, s13
	s_nop 0
	global_load_lds_dwordx4 v124, s[10:11]
	s_add_u32 s26, s10, 0x2000
	s_addc_u32 s27, s11, 0
	s_mov_b32 m0, s20
	s_nop 0
	global_load_lds_dwordx4 v124, s[26:27]
	global_load_dwordx4 v[96:99], v124, s[18:19]
	global_load_dwordx4 v[100:103], v124, s[18:19] offset:1024
	global_load_dwordx4 v[104:107], v124, s[18:19] offset:2048
	global_load_dwordx4 v[108:111], v124, s[22:23]
	global_load_dwordx4 v[112:115], v124, s[22:23] offset:1024
	global_load_dwordx4 v[116:119], v124, s[22:23] offset:2048
	s_add_u32 s24, s10, 0x3000
	s_addc_u32 s25, s11, 0
	s_add_u32 s26, s13, 0x3000
	s_mov_b32 m0, s26
	s_nop 0
	global_load_lds_dwordx4 v124, s[24:25]
	s_add_u32 s26, s24, 0x2000
	s_addc_u32 s27, s25, 0
	s_add_u32 s29, s20, 0x3000
	s_mov_b32 m0, s29
	s_nop 0
	global_load_lds_dwordx4 v124, s[26:27]
	s_add_u32 s24, s10, 0x6000
	s_addc_u32 s25, s11, 0
	s_add_u32 s26, s13, 0x6000
	s_mov_b32 m0, s26
	s_nop 0
	global_load_lds_dwordx4 v124, s[24:25]
	s_add_u32 s26, s24, 0x2000
	s_addc_u32 s27, s25, 0
	s_add_u32 s29, s20, 0x6000
	s_mov_b32 m0, s29
	s_nop 0
	global_load_lds_dwordx4 v124, s[26:27]
	s_add_u32 s24, s10, 0x9000
	s_addc_u32 s25, s11, 0
	s_add_u32 s26, s13, 0x9000
	s_mov_b32 m0, s26
	s_nop 0
	global_load_lds_dwordx4 v124, s[24:25]
	s_add_u32 s26, s24, 0x2000
	s_addc_u32 s27, s25, 0
	s_add_u32 s29, s20, 0x9000
	s_mov_b32 m0, s29
	s_nop 0
	global_load_lds_dwordx4 v124, s[26:27]
	s_add_u32 s24, s10, 0xc000
	s_addc_u32 s25, s11, 0
	s_add_u32 s26, s13, 0xc000
	s_mov_b32 m0, s26
	s_nop 0
	global_load_lds_dwordx4 v124, s[24:25]
	s_add_u32 s26, s24, 0x2000
	s_addc_u32 s27, s25, 0
	s_add_u32 s29, s20, 0xc000
	s_mov_b32 m0, s29
	s_nop 0
	global_load_lds_dwordx4 v124, s[26:27]
	s_waitcnt vmcnt(8)
	s_barrier
	ds_read_b128 v[0:3], v124
	ds_read_b128 v[4:7], v124 offset:1024
	ds_read_b128 v[8:11], v124 offset:2048
	ds_read_b128 v[12:15], v124 offset:3072
	ds_read_b128 v[16:19], v124 offset:4096
	ds_read_b128 v[20:23], v124 offset:5120
	s_setprio 2
	s_waitcnt lgkmcnt(4)
	v_mfma_f32_32x32x64_f8f6f4 v[48:63], v[0:5], v[96:101], 0 cbsz:2 blgp:2
	ds_read_b128 v[24:27], v124 offset:6144
	s_waitcnt lgkmcnt(4)
	v_mfma_f32_32x32x64_f8f6f4 v[48:63], v[6:11], v[102:107], v[48:63] cbsz:2 blgp:2
	ds_read_b128 v[28:31], v124 offset:7168
	ds_read_b128 v[32:35], v124 offset:8192
	s_waitcnt lgkmcnt(4)
	v_mfma_f32_32x32x64_f8f6f4 v[48:63], v[12:17], v[108:113], v[48:63] cbsz:2 blgp:2
	ds_read_b128 v[36:39], v124 offset:9216
	s_waitcnt lgkmcnt(4)
	v_mfma_f32_32x32x64_f8f6f4 v[48:63], v[18:23], v[114:119], v[48:63] cbsz:2 blgp:2
	ds_read_b128 v[40:43], v124 offset:10240
	ds_read_b128 v[44:47], v124 offset:11264
	s_waitcnt vmcnt(0) lgkmcnt(0)
	s_barrier
	s_add_u32 s24, s10, 0xf000
	s_addc_u32 s25, s11, 0
	s_mov_b32 m0, s13
	s_nop 0
	global_load_lds_dwordx4 v124, s[24:25]
	s_add_u32 s26, s24, 0x2000
	s_addc_u32 s27, s25, 0
	s_mov_b32 m0, s20
	s_nop 0
	global_load_lds_dwordx4 v124, s[26:27]
	v_mfma_f32_32x32x64_f8f6f4 v[64:79], v[24:29], v[96:101], 0 cbsz:2 blgp:2
	ds_read_b128 v[0:3], v124 offset:12288
	ds_read_b128 v[4:7], v124 offset:13312
	ds_read_b128 v[8:11], v124 offset:14336
	ds_read_b128 v[24:27], v124 offset:18432
	v_mfma_f32_32x32x64_f8f6f4 v[64:79], v[30:35], v[102:107], v[64:79] cbsz:2 blgp:2
	ds_read_b128 v[12:15], v124 offset:15360
	ds_read_b128 v[16:19], v124 offset:16384
	ds_read_b128 v[20:23], v124 offset:17408
	ds_read_b128 v[28:31], v124 offset:19456
	ds_read_b128 v[32:35], v124 offset:20480
	v_exp_f32_e32 v48, v48
	v_exp_f32_e32 v49, v49
	v_exp_f32_e32 v50, v50
	v_exp_f32_e32 v51, v51
	v_mfma_f32_32x32x64_f8f6f4 v[64:79], v[36:41], v[108:113], v[64:79] cbsz:2 blgp:2
	ds_read_b128 v[36:39], v124 offset:21504
	v_exp_f32_e32 v52, v52
	v_exp_f32_e32 v53, v53
	v_exp_f32_e32 v54, v54
	v_exp_f32_e32 v55, v55
	v_pk_add_f32 v[120:121], v[120:121], v[48:49]
	v_pk_add_f32 v[122:123], v[122:123], v[50:51]
	v_mfma_f32_32x32x64_f8f6f4 v[64:79], v[42:47], v[114:119], v[64:79] cbsz:2 blgp:2
	ds_read_b128 v[40:43], v124 offset:22528
	ds_read_b128 v[44:47], v124 offset:23552
	v_exp_f32_e32 v56, v56
	v_exp_f32_e32 v57, v57
	v_exp_f32_e32 v58, v58
	v_exp_f32_e32 v59, v59
	v_pk_add_f32 v[120:121], v[120:121], v[52:53]
	v_pk_add_f32 v[122:123], v[122:123], v[54:55]
	s_waitcnt lgkmcnt(5)
	v_mfma_f32_32x32x64_f8f6f4 v[80:95], v[0:5], v[96:101], 0 cbsz:2 blgp:2
	ds_read_b128 v[0:3], v124 offset:24576
	v_exp_f32_e32 v60, v60
	v_exp_f32_e32 v61, v61
	v_exp_f32_e32 v62, v62
	v_exp_f32_e32 v63, v63
	v_pk_add_f32 v[120:121], v[120:121], v[56:57]
	v_pk_add_f32 v[122:123], v[122:123], v[58:59]
	v_mfma_f32_32x32x64_f8f6f4 v[80:95], v[6:11], v[102:107], v[80:95] cbsz:2 blgp:2
	ds_read_b128 v[4:7], v124 offset:25600
	ds_read_b128 v[8:11], v124 offset:26624
	v_exp_f32_e32 v64, v64
	v_exp_f32_e32 v65, v65
	v_exp_f32_e32 v66, v66
	v_exp_f32_e32 v67, v67
	v_pk_add_f32 v[120:121], v[120:121], v[60:61]
	v_pk_add_f32 v[122:123], v[122:123], v[62:63]
	v_mfma_f32_32x32x64_f8f6f4 v[80:95], v[12:17], v[108:113], v[80:95] cbsz:2 blgp:2
	ds_read_b128 v[12:15], v124 offset:27648
	v_exp_f32_e32 v68, v68
	v_exp_f32_e32 v69, v69
	v_exp_f32_e32 v70, v70
	v_exp_f32_e32 v71, v71
	v_pk_add_f32 v[120:121], v[120:121], v[64:65]
	v_pk_add_f32 v[122:123], v[122:123], v[66:67]
	v_mfma_f32_32x32x64_f8f6f4 v[80:95], v[18:23], v[114:119], v[80:95] cbsz:2 blgp:2
	ds_read_b128 v[16:19], v124 offset:28672
	ds_read_b128 v[20:23], v124 offset:29696
	v_exp_f32_e32 v72, v72
	v_exp_f32_e32 v73, v73
	v_exp_f32_e32 v74, v74
	v_exp_f32_e32 v75, v75
	v_pk_add_f32 v[120:121], v[120:121], v[68:69]
	v_pk_add_f32 v[122:123], v[122:123], v[70:71]
	s_waitcnt lgkmcnt(6)
	v_mfma_f32_32x32x64_f8f6f4 v[48:63], v[24:29], v[96:101], 0 cbsz:2 blgp:2
	ds_read_b128 v[24:27], v124 offset:30720
	v_exp_f32_e32 v76, v76
	v_exp_f32_e32 v77, v77
	v_exp_f32_e32 v78, v78
	v_exp_f32_e32 v79, v79
	v_pk_add_f32 v[120:121], v[120:121], v[72:73]
	v_pk_add_f32 v[122:123], v[122:123], v[74:75]
	v_mfma_f32_32x32x64_f8f6f4 v[48:63], v[30:35], v[102:107], v[48:63] cbsz:2 blgp:2
	ds_read_b128 v[28:31], v124 offset:31744
	ds_read_b128 v[32:35], v124 offset:32768
	v_exp_f32_e32 v80, v80
	v_exp_f32_e32 v81, v81
	v_exp_f32_e32 v82, v82
	v_exp_f32_e32 v83, v83
	v_pk_add_f32 v[120:121], v[120:121], v[76:77]
	v_pk_add_f32 v[122:123], v[122:123], v[78:79]
	v_mfma_f32_32x32x64_f8f6f4 v[48:63], v[36:41], v[108:113], v[48:63] cbsz:2 blgp:2
	ds_read_b128 v[36:39], v124 offset:33792
	v_exp_f32_e32 v84, v84
	v_exp_f32_e32 v85, v85
	v_exp_f32_e32 v86, v86
	v_exp_f32_e32 v87, v87
	v_pk_add_f32 v[120:121], v[120:121], v[80:81]
	v_pk_add_f32 v[122:123], v[122:123], v[82:83]
	v_mfma_f32_32x32x64_f8f6f4 v[48:63], v[42:47], v[114:119], v[48:63] cbsz:2 blgp:2
	ds_read_b128 v[40:43], v124 offset:34816
	ds_read_b128 v[44:47], v124 offset:35840
	v_exp_f32_e32 v88, v88
	v_exp_f32_e32 v89, v89
	v_exp_f32_e32 v90, v90
	v_exp_f32_e32 v91, v91
	v_pk_add_f32 v[120:121], v[120:121], v[84:85]
	v_pk_add_f32 v[122:123], v[122:123], v[86:87]
	s_setprio 1
	s_waitcnt lgkmcnt(6)
	v_mfma_f32_32x32x64_f8f6f4 v[64:79], v[0:5], v[96:101], 0 cbsz:2 blgp:2
	ds_read_b128 v[0:3], v124 offset:36864
	v_exp_f32_e32 v92, v92
	v_exp_f32_e32 v93, v93
	v_exp_f32_e32 v94, v94
	v_exp_f32_e32 v95, v95
	v_pk_add_f32 v[120:121], v[120:121], v[88:89]
	v_pk_add_f32 v[122:123], v[122:123], v[90:91]
	v_mfma_f32_32x32x64_f8f6f4 v[64:79], v[6:11], v[102:107], v[64:79] cbsz:2 blgp:2
	ds_read_b128 v[4:7], v124 offset:37888
	ds_read_b128 v[8:11], v124 offset:38912
	v_exp_f32_e32 v48, v48
	v_exp_f32_e32 v49, v49
	v_exp_f32_e32 v50, v50
	v_exp_f32_e32 v51, v51
	v_pk_add_f32 v[120:121], v[120:121], v[92:93]
	v_pk_add_f32 v[122:123], v[122:123], v[94:95]
	v_mfma_f32_32x32x64_f8f6f4 v[64:79], v[12:17], v[108:113], v[64:79] cbsz:2 blgp:2
	ds_read_b128 v[12:15], v124 offset:39936
	v_exp_f32_e32 v52, v52
	v_exp_f32_e32 v53, v53
	v_exp_f32_e32 v54, v54
	v_exp_f32_e32 v55, v55
	v_pk_add_f32 v[120:121], v[120:121], v[48:49]
	v_pk_add_f32 v[122:123], v[122:123], v[50:51]
	v_mfma_f32_32x32x64_f8f6f4 v[64:79], v[18:23], v[114:119], v[64:79] cbsz:2 blgp:2
	ds_read_b128 v[16:19], v124 offset:40960
	ds_read_b128 v[20:23], v124 offset:41984
	v_exp_f32_e32 v56, v56
	v_exp_f32_e32 v57, v57
	v_exp_f32_e32 v58, v58
	v_exp_f32_e32 v59, v59
	v_pk_add_f32 v[120:121], v[120:121], v[52:53]
	v_pk_add_f32 v[122:123], v[122:123], v[54:55]
	s_waitcnt lgkmcnt(6)
	v_mfma_f32_32x32x64_f8f6f4 v[80:95], v[24:29], v[96:101], 0 cbsz:2 blgp:2
	ds_read_b128 v[24:27], v124 offset:43008
	v_exp_f32_e32 v60, v60
	v_exp_f32_e32 v61, v61
	v_exp_f32_e32 v62, v62
	v_exp_f32_e32 v63, v63
	v_pk_add_f32 v[120:121], v[120:121], v[56:57]
	v_pk_add_f32 v[122:123], v[122:123], v[58:59]
	v_mfma_f32_32x32x64_f8f6f4 v[80:95], v[30:35], v[102:107], v[80:95] cbsz:2 blgp:2
	ds_read_b128 v[28:31], v124 offset:44032
	ds_read_b128 v[32:35], v124 offset:45056
	v_exp_f32_e32 v64, v64
	v_exp_f32_e32 v65, v65
	v_exp_f32_e32 v66, v66
	v_exp_f32_e32 v67, v67
	v_pk_add_f32 v[120:121], v[120:121], v[60:61]
	v_pk_add_f32 v[122:123], v[122:123], v[62:63]
	v_mfma_f32_32x32x64_f8f6f4 v[80:95], v[36:41], v[108:113], v[80:95] cbsz:2 blgp:2
	ds_read_b128 v[36:39], v124 offset:46080
	v_exp_f32_e32 v68, v68
	v_exp_f32_e32 v69, v69
	v_exp_f32_e32 v70, v70
	v_exp_f32_e32 v71, v71
	v_pk_add_f32 v[120:121], v[120:121], v[64:65]
	v_pk_add_f32 v[122:123], v[122:123], v[66:67]
	v_mfma_f32_32x32x64_f8f6f4 v[80:95], v[42:47], v[114:119], v[80:95] cbsz:2 blgp:2
	ds_read_b128 v[40:43], v124 offset:47104
	ds_read_b128 v[44:47], v124 offset:48128
	v_exp_f32_e32 v72, v72
	v_exp_f32_e32 v73, v73
	v_exp_f32_e32 v74, v74
	v_exp_f32_e32 v75, v75
	v_pk_add_f32 v[120:121], v[120:121], v[68:69]
	v_pk_add_f32 v[122:123], v[122:123], v[70:71]
	s_waitcnt lgkmcnt(6)
	v_mfma_f32_32x32x64_f8f6f4 v[48:63], v[0:5], v[96:101], 0 cbsz:2 blgp:2
	ds_read_b128 v[0:3], v124 offset:49152
	v_exp_f32_e32 v76, v76
	v_exp_f32_e32 v77, v77
	v_exp_f32_e32 v78, v78
	v_exp_f32_e32 v79, v79
	v_pk_add_f32 v[120:121], v[120:121], v[72:73]
	v_pk_add_f32 v[122:123], v[122:123], v[74:75]
	v_mfma_f32_32x32x64_f8f6f4 v[48:63], v[6:11], v[102:107], v[48:63] cbsz:2 blgp:2
	ds_read_b128 v[4:7], v124 offset:50176
	ds_read_b128 v[8:11], v124 offset:51200
	v_exp_f32_e32 v80, v80
	v_exp_f32_e32 v81, v81
	v_exp_f32_e32 v82, v82
	v_exp_f32_e32 v83, v83
	v_pk_add_f32 v[120:121], v[120:121], v[76:77]
	v_pk_add_f32 v[122:123], v[122:123], v[78:79]
	v_mfma_f32_32x32x64_f8f6f4 v[48:63], v[12:17], v[108:113], v[48:63] cbsz:2 blgp:2
	ds_read_b128 v[12:15], v124 offset:52224
	v_exp_f32_e32 v84, v84
	v_exp_f32_e32 v85, v85
	v_exp_f32_e32 v86, v86
	v_exp_f32_e32 v87, v87
	v_pk_add_f32 v[120:121], v[120:121], v[80:81]
	v_pk_add_f32 v[122:123], v[122:123], v[82:83]
	v_mfma_f32_32x32x64_f8f6f4 v[48:63], v[18:23], v[114:119], v[48:63] cbsz:2 blgp:2
	ds_read_b128 v[16:19], v124 offset:53248
	ds_read_b128 v[20:23], v124 offset:54272
	v_exp_f32_e32 v88, v88
	v_exp_f32_e32 v89, v89
	v_exp_f32_e32 v90, v90
	v_exp_f32_e32 v91, v91
	v_pk_add_f32 v[120:121], v[120:121], v[84:85]
	v_pk_add_f32 v[122:123], v[122:123], v[86:87]
	s_waitcnt lgkmcnt(6)
	v_mfma_f32_32x32x64_f8f6f4 v[64:79], v[24:29], v[96:101], 0 cbsz:2 blgp:2
	ds_read_b128 v[24:27], v124 offset:55296
	v_exp_f32_e32 v92, v92
	v_exp_f32_e32 v93, v93
	v_exp_f32_e32 v94, v94
	v_exp_f32_e32 v95, v95
	v_pk_add_f32 v[120:121], v[120:121], v[88:89]
	v_pk_add_f32 v[122:123], v[122:123], v[90:91]
	v_mfma_f32_32x32x64_f8f6f4 v[64:79], v[30:35], v[102:107], v[64:79] cbsz:2 blgp:2
	ds_read_b128 v[28:31], v124 offset:56320
	ds_read_b128 v[32:35], v124 offset:57344
	v_exp_f32_e32 v48, v48
	v_exp_f32_e32 v49, v49
	v_exp_f32_e32 v50, v50
	v_exp_f32_e32 v51, v51
	v_pk_add_f32 v[120:121], v[120:121], v[92:93]
	v_pk_add_f32 v[122:123], v[122:123], v[94:95]
	v_mfma_f32_32x32x64_f8f6f4 v[64:79], v[36:41], v[108:113], v[64:79] cbsz:2 blgp:2
	ds_read_b128 v[36:39], v124 offset:58368
	v_exp_f32_e32 v52, v52
	v_exp_f32_e32 v53, v53
	v_exp_f32_e32 v54, v54
	v_exp_f32_e32 v55, v55
	v_pk_add_f32 v[120:121], v[120:121], v[48:49]
	v_pk_add_f32 v[122:123], v[122:123], v[50:51]
	v_mfma_f32_32x32x64_f8f6f4 v[64:79], v[42:47], v[114:119], v[64:79] cbsz:2 blgp:2
	ds_read_b128 v[40:43], v124 offset:59392
	ds_read_b128 v[44:47], v124 offset:60416
	v_exp_f32_e32 v56, v56
	v_exp_f32_e32 v57, v57
	v_exp_f32_e32 v58, v58
	v_exp_f32_e32 v59, v59
	v_pk_add_f32 v[120:121], v[120:121], v[52:53]
	v_pk_add_f32 v[122:123], v[122:123], v[54:55]
	s_setprio 0
	s_waitcnt vmcnt(0) lgkmcnt(6)
	s_barrier
	v_mfma_f32_32x32x64_f8f6f4 v[80:95], v[0:5], v[96:101], 0 cbsz:2 blgp:2
	ds_read_b128 v[0:3], v124
	v_exp_f32_e32 v60, v60
	v_exp_f32_e32 v61, v61
	v_exp_f32_e32 v62, v62
	v_exp_f32_e32 v63, v63
	v_pk_add_f32 v[120:121], v[120:121], v[56:57]
	v_pk_add_f32 v[122:123], v[122:123], v[58:59]
	v_mfma_f32_32x32x64_f8f6f4 v[80:95], v[6:11], v[102:107], v[80:95] cbsz:2 blgp:2
	ds_read_b128 v[4:7], v124 offset:1024
	ds_read_b128 v[8:11], v124 offset:2048
	v_exp_f32_e32 v64, v64
	v_exp_f32_e32 v65, v65
	v_exp_f32_e32 v66, v66
	v_exp_f32_e32 v67, v67
	v_pk_add_f32 v[120:121], v[120:121], v[60:61]
	v_pk_add_f32 v[122:123], v[122:123], v[62:63]
	v_mfma_f32_32x32x64_f8f6f4 v[80:95], v[12:17], v[108:113], v[80:95] cbsz:2 blgp:2
	ds_read_b128 v[12:15], v124 offset:3072
	v_exp_f32_e32 v68, v68
	v_exp_f32_e32 v69, v69
	v_exp_f32_e32 v70, v70
	v_exp_f32_e32 v71, v71
	v_pk_add_f32 v[120:121], v[120:121], v[64:65]
	v_pk_add_f32 v[122:123], v[122:123], v[66:67]
	v_mfma_f32_32x32x64_f8f6f4 v[80:95], v[18:23], v[114:119], v[80:95] cbsz:2 blgp:2
	ds_read_b128 v[16:19], v124 offset:4096
	ds_read_b128 v[20:23], v124 offset:5120
	v_exp_f32_e32 v72, v72
	v_exp_f32_e32 v73, v73
	v_exp_f32_e32 v74, v74
	v_exp_f32_e32 v75, v75
	v_pk_add_f32 v[120:121], v[120:121], v[68:69]
	v_pk_add_f32 v[122:123], v[122:123], v[70:71]
	s_waitcnt lgkmcnt(6)
	v_mfma_f32_32x32x64_f8f6f4 v[48:63], v[24:29], v[96:101], 0 cbsz:2 blgp:2
	ds_read_b128 v[24:27], v124 offset:6144
	v_exp_f32_e32 v76, v76
	v_exp_f32_e32 v77, v77
	v_exp_f32_e32 v78, v78
	v_exp_f32_e32 v79, v79
	v_pk_add_f32 v[120:121], v[120:121], v[72:73]
	v_pk_add_f32 v[122:123], v[122:123], v[74:75]
	v_mfma_f32_32x32x64_f8f6f4 v[48:63], v[30:35], v[102:107], v[48:63] cbsz:2 blgp:2
	ds_read_b128 v[28:31], v124 offset:7168
	ds_read_b128 v[32:35], v124 offset:8192
	v_exp_f32_e32 v80, v80
	v_exp_f32_e32 v81, v81
	v_exp_f32_e32 v82, v82
	v_exp_f32_e32 v83, v83
	v_pk_add_f32 v[120:121], v[120:121], v[76:77]
	v_pk_add_f32 v[122:123], v[122:123], v[78:79]
	s_cmp_lg_u32 s8, 10
	s_cbranch_scc1 .Lmk_nosplit_a
	v_add_f32_e32 v127, v120, v121
	v_add_f32_e32 v126, v122, v123
	v_mov_b32_e32 v120, 0
	v_mov_b32_e32 v121, 0
	v_mov_b32_e32 v122, 0
	v_mov_b32_e32 v123, 0
	v_add_f32_e32 v127, v127, v126

.Lmk_vb:
	s_mov_b32 m0, s13
	s_nop 0
	global_load_lds_dwordx4 v124, s[10:11]
	global_load_dwordx4 v[96:99], v124, s[18:19]
	global_load_dwordx4 v[100:103], v124, s[18:19] offset:1024
	global_load_dwordx4 v[104:107], v124, s[18:19] offset:2048
	global_load_dwordx4 v[108:111], v124, s[22:23]
	global_load_dwordx4 v[112:115], v124, s[22:23] offset:1024
	global_load_dwordx4 v[116:119], v124, s[22:23] offset:2048
	s_add_u32 s24, s10, 0x3000
	s_addc_u32 s25, s11, 0
	s_add_u32 s26, s13, 0x3000
	s_mov_b32 m0, s26
	s_nop 0
	global_load_lds_dwordx4 v124, s[24:25]
	s_add_u32 s24, s10, 0x6000
	s_addc_u32 s25, s11, 0
	s_add_u32 s26, s13, 0x6000
	s_mov_b32 m0, s26
	s_nop 0
	global_load_lds_dwordx4 v124, s[24:25]
	s_add_u32 s24, s10, 0x9000
	s_addc_u32 s25, s11, 0
	s_add_u32 s26, s13, 0x9000
	s_mov_b32 m0, s26
	s_nop 0
	global_load_lds_dwordx4 v124, s[24:25]
	s_add_u32 s24, s10, 0xc000
	s_addc_u32 s25, s11, 0
	s_add_u32 s26, s13, 0xc000
	s_mov_b32 m0, s26
	s_nop 0
	global_load_lds_dwordx4 v124, s[24:25]
	s_waitcnt vmcnt(4)
	s_barrier
	ds_read_b128 v[0:3], v124
	ds_read_b128 v[4:7], v124 offset:1024
	ds_read_b128 v[8:11], v124 offset:2048
	ds_read_b128 v[12:15], v124 offset:3072
	ds_read_b128 v[16:19], v124 offset:4096
	ds_read_b128 v[20:23], v124 offset:5120
	s_setprio 3
	s_waitcnt lgkmcnt(4)
	v_mfma_f32_32x32x64_f8f6f4 v[48:63], v[0:5], v[96:101], 0 cbsz:2 blgp:2
	ds_read_b128 v[24:27], v124 offset:6144
	s_waitcnt lgkmcnt(4)
	v_mfma_f32_32x32x64_f8f6f4 v[48:63], v[6:11], v[102:107], v[48:63] cbsz:2 blgp:2
	ds_read_b128 v[28:31], v124 offset:7168
	ds_read_b128 v[32:35], v124 offset:8192
	s_waitcnt lgkmcnt(4)
	v_mfma_f32_32x32x64_f8f6f4 v[48:63], v[12:17], v[108:113], v[48:63] cbsz:2 blgp:2
	ds_read_b128 v[36:39], v124 offset:9216
	s_waitcnt lgkmcnt(4)
	v_mfma_f32_32x32x64_f8f6f4 v[48:63], v[18:23], v[114:119], v[48:63] cbsz:2 blgp:2
	ds_read_b128 v[40:43], v124 offset:10240
	ds_read_b128 v[44:47], v124 offset:11264
	s_waitcnt vmcnt(0) lgkmcnt(0)
	s_barrier
	s_add_u32 s24, s10, 0xf000
	s_addc_u32 s25, s11, 0
	s_mov_b32 m0, s13
	s_nop 0
	global_load_lds_dwordx4 v124, s[24:25]
	v_mfma_f32_32x32x64_f8f6f4 v[64:79], v[24:29], v[96:101], 0 cbsz:2 blgp:2
	ds_read_b128 v[0:3], v124 offset:12288
	ds_read_b128 v[4:7], v124 offset:13312
	ds_read_b128 v[8:11], v124 offset:14336
	ds_read_b128 v[24:27], v124 offset:18432
	v_mfma_f32_32x32x64_f8f6f4 v[64:79], v[30:35], v[102:107], v[64:79] cbsz:2 blgp:2
	ds_read_b128 v[12:15], v124 offset:15360
	ds_read_b128 v[16:19], v124 offset:16384
	ds_read_b128 v[20:23], v124 offset:17408
	ds_read_b128 v[28:31], v124 offset:19456
	ds_read_b128 v[32:35], v124 offset:20480
	v_exp_f32_e32 v48, v48
	v_exp_f32_e32 v49, v49
	v_exp_f32_e32 v50, v50
	v_exp_f32_e32 v51, v51
	v_mfma_f32_32x32x64_f8f6f4 v[64:79], v[36:41], v[108:113], v[64:79] cbsz:2 blgp:2
	ds_read_b128 v[36:39], v124 offset:21504
	v_exp_f32_e32 v52, v52
	v_exp_f32_e32 v53, v53
	v_exp_f32_e32 v54, v54
	v_exp_f32_e32 v55, v55
	v_pk_add_f32 v[120:121], v[120:121], v[48:49]
	v_pk_add_f32 v[122:123], v[122:123], v[50:51]
	v_mfma_f32_32x32x64_f8f6f4 v[64:79], v[42:47], v[114:119], v[64:79] cbsz:2 blgp:2
	ds_read_b128 v[40:43], v124 offset:22528
	ds_read_b128 v[44:47], v124 offset:23552
	v_exp_f32_e32 v56, v56
	v_exp_f32_e32 v57, v57
	v_exp_f32_e32 v58, v58
	v_exp_f32_e32 v59, v59
	v_pk_add_f32 v[120:121], v[120:121], v[52:53]
	v_pk_add_f32 v[122:123], v[122:123], v[54:55]
	s_waitcnt lgkmcnt(5)
	v_mfma_f32_32x32x64_f8f6f4 v[80:95], v[0:5], v[96:101], 0 cbsz:2 blgp:2
	ds_read_b128 v[0:3], v124 offset:24576
	v_exp_f32_e32 v60, v60
	v_exp_f32_e32 v61, v61
	v_exp_f32_e32 v62, v62
	v_exp_f32_e32 v63, v63
	v_pk_add_f32 v[120:121], v[120:121], v[56:57]
	v_pk_add_f32 v[122:123], v[122:123], v[58:59]
	v_mfma_f32_32x32x64_f8f6f4 v[80:95], v[6:11], v[102:107], v[80:95] cbsz:2 blgp:2
	ds_read_b128 v[4:7], v124 offset:25600
	ds_read_b128 v[8:11], v124 offset:26624
	v_exp_f32_e32 v64, v64
	v_exp_f32_e32 v65, v65
	v_exp_f32_e32 v66, v66
	v_exp_f32_e32 v67, v67
	v_pk_add_f32 v[120:121], v[120:121], v[60:61]
	v_pk_add_f32 v[122:123], v[122:123], v[62:63]
	v_mfma_f32_32x32x64_f8f6f4 v[80:95], v[12:17], v[108:113], v[80:95] cbsz:2 blgp:2
	ds_read_b128 v[12:15], v124 offset:27648
	v_exp_f32_e32 v68, v68
	v_exp_f32_e32 v69, v69
	v_exp_f32_e32 v70, v70
	v_exp_f32_e32 v71, v71
	v_pk_add_f32 v[120:121], v[120:121], v[64:65]
	v_pk_add_f32 v[122:123], v[122:123], v[66:67]
	v_mfma_f32_32x32x64_f8f6f4 v[80:95], v[18:23], v[114:119], v[80:95] cbsz:2 blgp:2
	ds_read_b128 v[16:19], v124 offset:28672
	ds_read_b128 v[20:23], v124 offset:29696
	v_exp_f32_e32 v72, v72
	v_exp_f32_e32 v73, v73
	v_exp_f32_e32 v74, v74
	v_exp_f32_e32 v75, v75
	v_pk_add_f32 v[120:121], v[120:121], v[68:69]
	v_pk_add_f32 v[122:123], v[122:123], v[70:71]
	s_waitcnt lgkmcnt(6)
	v_mfma_f32_32x32x64_f8f6f4 v[48:63], v[24:29], v[96:101], 0 cbsz:2 blgp:2
	ds_read_b128 v[24:27], v124 offset:30720
	v_exp_f32_e32 v76, v76
	v_exp_f32_e32 v77, v77
	v_exp_f32_e32 v78, v78
	v_exp_f32_e32 v79, v79
	v_pk_add_f32 v[120:121], v[120:121], v[72:73]
	v_pk_add_f32 v[122:123], v[122:123], v[74:75]
	v_mfma_f32_32x32x64_f8f6f4 v[48:63], v[30:35], v[102:107], v[48:63] cbsz:2 blgp:2
	ds_read_b128 v[28:31], v124 offset:31744
	ds_read_b128 v[32:35], v124 offset:32768
	v_exp_f32_e32 v80, v80
	v_exp_f32_e32 v81, v81
	v_exp_f32_e32 v82, v82
	v_exp_f32_e32 v83, v83
	v_pk_add_f32 v[120:121], v[120:121], v[76:77]
	v_pk_add_f32 v[122:123], v[122:123], v[78:79]
	v_mfma_f32_32x32x64_f8f6f4 v[48:63], v[36:41], v[108:113], v[48:63] cbsz:2 blgp:2
	ds_read_b128 v[36:39], v124 offset:33792
	v_exp_f32_e32 v84, v84
	v_exp_f32_e32 v85, v85
	v_exp_f32_e32 v86, v86
	v_exp_f32_e32 v87, v87
	v_pk_add_f32 v[120:121], v[120:121], v[80:81]
	v_pk_add_f32 v[122:123], v[122:123], v[82:83]
	v_mfma_f32_32x32x64_f8f6f4 v[48:63], v[42:47], v[114:119], v[48:63] cbsz:2 blgp:2
	ds_read_b128 v[40:43], v124 offset:34816
	ds_read_b128 v[44:47], v124 offset:35840
	v_exp_f32_e32 v88, v88
	v_exp_f32_e32 v89, v89
	v_exp_f32_e32 v90, v90
	v_exp_f32_e32 v91, v91
	v_pk_add_f32 v[120:121], v[120:121], v[84:85]
	v_pk_add_f32 v[122:123], v[122:123], v[86:87]
	s_setprio 2
	s_waitcnt lgkmcnt(6)
	v_mfma_f32_32x32x64_f8f6f4 v[64:79], v[0:5], v[96:101], 0 cbsz:2 blgp:2
	ds_read_b128 v[0:3], v124 offset:36864
	v_exp_f32_e32 v92, v92
	v_exp_f32_e32 v93, v93
	v_exp_f32_e32 v94, v94
	v_exp_f32_e32 v95, v95
	v_pk_add_f32 v[120:121], v[120:121], v[88:89]
	v_pk_add_f32 v[122:123], v[122:123], v[90:91]
	v_mfma_f32_32x32x64_f8f6f4 v[64:79], v[6:11], v[102:107], v[64:79] cbsz:2 blgp:2
	ds_read_b128 v[4:7], v124 offset:37888
	ds_read_b128 v[8:11], v124 offset:38912
	v_exp_f32_e32 v48, v48
	v_exp_f32_e32 v49, v49
	v_exp_f32_e32 v50, v50
	v_exp_f32_e32 v51, v51
	v_pk_add_f32 v[120:121], v[120:121], v[92:93]
	v_pk_add_f32 v[122:123], v[122:123], v[94:95]
	v_mfma_f32_32x32x64_f8f6f4 v[64:79], v[12:17], v[108:113], v[64:79] cbsz:2 blgp:2
	ds_read_b128 v[12:15], v124 offset:39936
	v_exp_f32_e32 v52, v52
	v_exp_f32_e32 v53, v53
	v_exp_f32_e32 v54, v54
	v_exp_f32_e32 v55, v55
	v_pk_add_f32 v[120:121], v[120:121], v[48:49]
	v_pk_add_f32 v[122:123], v[122:123], v[50:51]
	v_mfma_f32_32x32x64_f8f6f4 v[64:79], v[18:23], v[114:119], v[64:79] cbsz:2 blgp:2
	ds_read_b128 v[16:19], v124 offset:40960
	ds_read_b128 v[20:23], v124 offset:41984
	v_exp_f32_e32 v56, v56
	v_exp_f32_e32 v57, v57
	v_exp_f32_e32 v58, v58
	v_exp_f32_e32 v59, v59
	v_pk_add_f32 v[120:121], v[120:121], v[52:53]
	v_pk_add_f32 v[122:123], v[122:123], v[54:55]
	s_waitcnt lgkmcnt(6)
	v_mfma_f32_32x32x64_f8f6f4 v[80:95], v[24:29], v[96:101], 0 cbsz:2 blgp:2
	ds_read_b128 v[24:27], v124 offset:43008
	v_exp_f32_e32 v60, v60
	v_exp_f32_e32 v61, v61
	v_exp_f32_e32 v62, v62
	v_exp_f32_e32 v63, v63
	v_pk_add_f32 v[120:121], v[120:121], v[56:57]
	v_pk_add_f32 v[122:123], v[122:123], v[58:59]
	v_mfma_f32_32x32x64_f8f6f4 v[80:95], v[30:35], v[102:107], v[80:95] cbsz:2 blgp:2
	ds_read_b128 v[28:31], v124 offset:44032
	ds_read_b128 v[32:35], v124 offset:45056
	v_exp_f32_e32 v64, v64
	v_exp_f32_e32 v65, v65
	v_exp_f32_e32 v66, v66
	v_exp_f32_e32 v67, v67
	v_pk_add_f32 v[120:121], v[120:121], v[60:61]
	v_pk_add_f32 v[122:123], v[122:123], v[62:63]
	v_mfma_f32_32x32x64_f8f6f4 v[80:95], v[36:41], v[108:113], v[80:95] cbsz:2 blgp:2
	ds_read_b128 v[36:39], v124 offset:46080
	v_exp_f32_e32 v68, v68
	v_exp_f32_e32 v69, v69
	v_exp_f32_e32 v70, v70
	v_exp_f32_e32 v71, v71
	v_pk_add_f32 v[120:121], v[120:121], v[64:65]
	v_pk_add_f32 v[122:123], v[122:123], v[66:67]
	v_mfma_f32_32x32x64_f8f6f4 v[80:95], v[42:47], v[114:119], v[80:95] cbsz:2 blgp:2
	ds_read_b128 v[40:43], v124 offset:47104
	ds_read_b128 v[44:47], v124 offset:48128
	v_exp_f32_e32 v72, v72
	v_exp_f32_e32 v73, v73
	v_exp_f32_e32 v74, v74
	v_exp_f32_e32 v75, v75
	v_pk_add_f32 v[120:121], v[120:121], v[68:69]
	v_pk_add_f32 v[122:123], v[122:123], v[70:71]
	s_waitcnt lgkmcnt(6)
	v_mfma_f32_32x32x64_f8f6f4 v[48:63], v[0:5], v[96:101], 0 cbsz:2 blgp:2
	ds_read_b128 v[0:3], v124 offset:49152
	v_exp_f32_e32 v76, v76
	v_exp_f32_e32 v77, v77
	v_exp_f32_e32 v78, v78
	v_exp_f32_e32 v79, v79
	v_pk_add_f32 v[120:121], v[120:121], v[72:73]
	v_pk_add_f32 v[122:123], v[122:123], v[74:75]
	v_mfma_f32_32x32x64_f8f6f4 v[48:63], v[6:11], v[102:107], v[48:63] cbsz:2 blgp:2
	ds_read_b128 v[4:7], v124 offset:50176
	ds_read_b128 v[8:11], v124 offset:51200
	v_exp_f32_e32 v80, v80
	v_exp_f32_e32 v81, v81
	v_exp_f32_e32 v82, v82
	v_exp_f32_e32 v83, v83
	v_pk_add_f32 v[120:121], v[120:121], v[76:77]
	v_pk_add_f32 v[122:123], v[122:123], v[78:79]
	v_mfma_f32_32x32x64_f8f6f4 v[48:63], v[12:17], v[108:113], v[48:63] cbsz:2 blgp:2
	ds_read_b128 v[12:15], v124 offset:52224
	v_exp_f32_e32 v84, v84
	v_exp_f32_e32 v85, v85
	v_exp_f32_e32 v86, v86
	v_exp_f32_e32 v87, v87
	v_pk_add_f32 v[120:121], v[120:121], v[80:81]
	v_pk_add_f32 v[122:123], v[122:123], v[82:83]
	v_mfma_f32_32x32x64_f8f6f4 v[48:63], v[18:23], v[114:119], v[48:63] cbsz:2 blgp:2
	ds_read_b128 v[16:19], v124 offset:53248
	ds_read_b128 v[20:23], v124 offset:54272
	v_exp_f32_e32 v88, v88
	v_exp_f32_e32 v89, v89
	v_exp_f32_e32 v90, v90
	v_exp_f32_e32 v91, v91
	v_pk_add_f32 v[120:121], v[120:121], v[84:85]
	v_pk_add_f32 v[122:123], v[122:123], v[86:87]
	s_waitcnt lgkmcnt(6)
	v_mfma_f32_32x32x64_f8f6f4 v[64:79], v[24:29], v[96:101], 0 cbsz:2 blgp:2
	ds_read_b128 v[24:27], v124 offset:55296
	v_exp_f32_e32 v92, v92
	v_exp_f32_e32 v93, v93
	v_exp_f32_e32 v94, v94
	v_exp_f32_e32 v95, v95
	v_pk_add_f32 v[120:121], v[120:121], v[88:89]
	v_pk_add_f32 v[122:123], v[122:123], v[90:91]
	v_mfma_f32_32x32x64_f8f6f4 v[64:79], v[30:35], v[102:107], v[64:79] cbsz:2 blgp:2
	ds_read_b128 v[28:31], v124 offset:56320
	ds_read_b128 v[32:35], v124 offset:57344
	v_exp_f32_e32 v48, v48
	v_exp_f32_e32 v49, v49
	v_exp_f32_e32 v50, v50
	v_exp_f32_e32 v51, v51
	v_pk_add_f32 v[120:121], v[120:121], v[92:93]
	v_pk_add_f32 v[122:123], v[122:123], v[94:95]
	v_mfma_f32_32x32x64_f8f6f4 v[64:79], v[36:41], v[108:113], v[64:79] cbsz:2 blgp:2
	ds_read_b128 v[36:39], v124 offset:58368
	v_exp_f32_e32 v52, v52
	v_exp_f32_e32 v53, v53
	v_exp_f32_e32 v54, v54
	v_exp_f32_e32 v55, v55
	v_pk_add_f32 v[120:121], v[120:121], v[48:49]
	v_pk_add_f32 v[122:123], v[122:123], v[50:51]
	v_mfma_f32_32x32x64_f8f6f4 v[64:79], v[42:47], v[114:119], v[64:79] cbsz:2 blgp:2
	ds_read_b128 v[40:43], v124 offset:59392
	ds_read_b128 v[44:47], v124 offset:60416
	v_exp_f32_e32 v56, v56
	v_exp_f32_e32 v57, v57
	v_exp_f32_e32 v58, v58
	v_exp_f32_e32 v59, v59
	v_pk_add_f32 v[120:121], v[120:121], v[52:53]
	v_pk_add_f32 v[122:123], v[122:123], v[54:55]
	s_setprio 1
	s_waitcnt vmcnt(0) lgkmcnt(6)
	s_barrier
	v_mfma_f32_32x32x64_f8f6f4 v[80:95], v[0:5], v[96:101], 0 cbsz:2 blgp:2
	ds_read_b128 v[0:3], v124
	v_exp_f32_e32 v60, v60
	v_exp_f32_e32 v61, v61
	v_exp_f32_e32 v62, v62
	v_exp_f32_e32 v63, v63
	v_pk_add_f32 v[120:121], v[120:121], v[56:57]
	v_pk_add_f32 v[122:123], v[122:123], v[58:59]
	v_mfma_f32_32x32x64_f8f6f4 v[80:95], v[6:11], v[102:107], v[80:95] cbsz:2 blgp:2
	ds_read_b128 v[4:7], v124 offset:1024
	ds_read_b128 v[8:11], v124 offset:2048
	v_exp_f32_e32 v64, v64
	v_exp_f32_e32 v65, v65
	v_exp_f32_e32 v66, v66
	v_exp_f32_e32 v67, v67
	v_pk_add_f32 v[120:121], v[120:121], v[60:61]
	v_pk_add_f32 v[122:123], v[122:123], v[62:63]
	v_mfma_f32_32x32x64_f8f6f4 v[80:95], v[12:17], v[108:113], v[80:95] cbsz:2 blgp:2
	ds_read_b128 v[12:15], v124 offset:3072
	v_exp_f32_e32 v68, v68
	v_exp_f32_e32 v69, v69
	v_exp_f32_e32 v70, v70
	v_exp_f32_e32 v71, v71
	v_pk_add_f32 v[120:121], v[120:121], v[64:65]
	v_pk_add_f32 v[122:123], v[122:123], v[66:67]
	v_mfma_f32_32x32x64_f8f6f4 v[80:95], v[18:23], v[114:119], v[80:95] cbsz:2 blgp:2
	ds_read_b128 v[16:19], v124 offset:4096
	ds_read_b128 v[20:23], v124 offset:5120
	v_exp_f32_e32 v72, v72
	v_exp_f32_e32 v73, v73
	v_exp_f32_e32 v74, v74
	v_exp_f32_e32 v75, v75
	v_pk_add_f32 v[120:121], v[120:121], v[68:69]
	v_pk_add_f32 v[122:123], v[122:123], v[70:71]
	s_waitcnt lgkmcnt(6)
	v_mfma_f32_32x32x64_f8f6f4 v[48:63], v[24:29], v[96:101], 0 cbsz:2 blgp:2
	ds_read_b128 v[24:27], v124 offset:6144
	v_exp_f32_e32 v76, v76
	v_exp_f32_e32 v77, v77
	v_exp_f32_e32 v78, v78
	v_exp_f32_e32 v79, v79
	v_pk_add_f32 v[120:121], v[120:121], v[72:73]
	v_pk_add_f32 v[122:123], v[122:123], v[74:75]
	v_mfma_f32_32x32x64_f8f6f4 v[48:63], v[30:35], v[102:107], v[48:63] cbsz:2 blgp:2
	ds_read_b128 v[28:31], v124 offset:7168
	ds_read_b128 v[32:35], v124 offset:8192
	v_exp_f32_e32 v80, v80
	v_exp_f32_e32 v81, v81
	v_exp_f32_e32 v82, v82
	v_exp_f32_e32 v83, v83
	v_pk_add_f32 v[120:121], v[120:121], v[76:77]
	v_pk_add_f32 v[122:123], v[122:123], v[78:79]
	s_cmp_lg_u32 s8, 10
	s_cbranch_scc1 .Lmk_nosplit_b
	v_add_f32_e32 v127, v120, v121
	v_add_f32_e32 v126, v122, v123
	v_mov_b32_e32 v120, 0
	v_mov_b32_e32 v121, 0
	v_mov_b32_e32 v122, 0
	v_mov_b32_e32 v123, 0
	v_add_f32_e32 v127, v127, v126
